# attention QK^T: K-fragment ds_reads issued three MFMA steps ahead (counted lgkmcnt) instead of read-then-wait per step; stacked on previous
# speedup vs baseline: 1.0157x; 1.0049x over previous
.LBB0_1165:
	s_cmp_ge_i32 s15, s59
	s_cbranch_scc1 .LBB0_1169
	s_lshl_b32 s61, s61, 14
	v_add_u32_e32 v1, s61, v180
	v_add_u32_e32 v70, v1, v181
	ds_read_b128 v[66:69], v70 offset:32768
	ds_read_b128 v[70:73], v70 offset:40960
	v_add_u32_e32 v170, v1, v182
	ds_read_b128 v[202:205], v170 offset:32768
	ds_read_b128 v[206:209], v170 offset:40960
	v_add_u32_e32 v170, v1, v183
	ds_read_b128 v[238:241], v170 offset:32768
	ds_read_b128 v[242:245], v170 offset:40960
	v_add_u32_e32 v170, v1, v184
	ds_read_b128 v[246:249], v170 offset:32768
	ds_read_b128 v[250:253], v170 offset:40960
	s_add_i32 s62, s15, 63
	s_cmp_lt_i32 s62, s14
	s_waitcnt lgkmcnt(7)
	v_mfma_f32_32x32x16_bf16 v[82:97], v[66:69], v[98:101], 0
	s_waitcnt lgkmcnt(6)
	v_mfma_f32_32x32x16_bf16 v[66:81], v[70:73], v[98:101], 0
	s_waitcnt lgkmcnt(5)
	v_mfma_f32_32x32x16_bf16 v[82:97], v[202:205], v[102:105], v[82:97]
	s_waitcnt lgkmcnt(4)
	v_mfma_f32_32x32x16_bf16 v[66:81], v[206:209], v[102:105], v[66:81]
	v_add_u32_e32 v170, v1, v185
	ds_read_b128 v[202:205], v170 offset:32768
	ds_read_b128 v[206:209], v170 offset:40960
	s_waitcnt lgkmcnt(5)
	v_mfma_f32_32x32x16_bf16 v[82:97], v[238:241], v[106:109], v[82:97]
	s_waitcnt lgkmcnt(4)
	v_mfma_f32_32x32x16_bf16 v[66:81], v[242:245], v[106:109], v[66:81]
	v_add_u32_e32 v170, v1, v186
	ds_read_b128 v[238:241], v170 offset:32768
	ds_read_b128 v[242:245], v170 offset:40960
	s_waitcnt lgkmcnt(5)
	v_mfma_f32_32x32x16_bf16 v[82:97], v[246:249], v[110:113], v[82:97]
	s_waitcnt lgkmcnt(4)
	v_mfma_f32_32x32x16_bf16 v[66:81], v[250:253], v[110:113], v[66:81]
	v_add_u32_e32 v170, v1, v187
	ds_read_b128 v[246:249], v170 offset:32768
	ds_read_b128 v[250:253], v170 offset:40960
	s_waitcnt lgkmcnt(5)
	v_mfma_f32_32x32x16_bf16 v[82:97], v[202:205], v[114:117], v[82:97]
	s_waitcnt lgkmcnt(4)
	v_mfma_f32_32x32x16_bf16 v[66:81], v[206:209], v[114:117], v[66:81]
	v_add_u32_e32 v170, v1, v188
	ds_read_b128 v[202:205], v170 offset:32768
	ds_read_b128 v[206:209], v170 offset:40960
	s_waitcnt lgkmcnt(5)
	v_mfma_f32_32x32x16_bf16 v[82:97], v[238:241], v[118:121], v[82:97]
	s_waitcnt lgkmcnt(4)
	v_mfma_f32_32x32x16_bf16 v[66:81], v[242:245], v[118:121], v[66:81]
	s_waitcnt lgkmcnt(3)
	v_mfma_f32_32x32x16_bf16 v[82:97], v[246:249], v[122:125], v[82:97]
	s_waitcnt lgkmcnt(2)
	v_mfma_f32_32x32x16_bf16 v[66:81], v[250:253], v[122:125], v[66:81]
	s_waitcnt lgkmcnt(1)
	v_mfma_f32_32x32x16_bf16 v[82:97], v[202:205], v[126:129], v[82:97]
	s_waitcnt lgkmcnt(0)
	v_mfma_f32_32x32x16_bf16 v[66:81], v[206:209], v[126:129], v[66:81]
	s_cbranch_scc1 .LBB0_1168
	v_add_u32_e32 v1, s15, v189
	v_cmp_lt_i32_e32 vcc, v1, v200
	v_add_u32_e32 v170, 32, v1
	s_nop 5
	v_cndmask_b32_e32 v82, v199, v82, vcc
	v_cmp_lt_i32_e32 vcc, v170, v200
	v_add_u32_e32 v170, 1, v1
	s_nop 0
	v_cndmask_b32_e32 v66, v199, v66, vcc
	v_cmp_lt_i32_e32 vcc, v170, v200
	v_add_u32_e32 v170, 33, v1
	s_nop 0
	v_cndmask_b32_e32 v83, v199, v83, vcc
	v_cmp_lt_i32_e32 vcc, v170, v200
	v_add_u32_e32 v170, 2, v1
	s_nop 0
	v_cndmask_b32_e32 v67, v199, v67, vcc
	v_cmp_lt_i32_e32 vcc, v170, v200
	v_add_u32_e32 v170, 34, v1
	s_nop 0
	v_cndmask_b32_e32 v84, v199, v84, vcc
	v_cmp_lt_i32_e32 vcc, v170, v200
	v_add_u32_e32 v170, 3, v1
	s_nop 0
	v_cndmask_b32_e32 v68, v199, v68, vcc
	v_cmp_lt_i32_e32 vcc, v170, v200
	v_add_u32_e32 v170, 35, v1
	s_nop 0
	v_cndmask_b32_e32 v85, v199, v85, vcc
	v_cmp_lt_i32_e32 vcc, v170, v200
	v_add_u32_e32 v170, 8, v1
	s_nop 0
	v_cndmask_b32_e32 v69, v199, v69, vcc
	v_cmp_lt_i32_e32 vcc, v170, v200
	v_add_u32_e32 v170, 40, v1
	s_nop 0
	v_cndmask_b32_e32 v86, v199, v86, vcc
	v_cmp_lt_i32_e32 vcc, v170, v200
	v_add_u32_e32 v170, 9, v1
	s_nop 0
	v_cndmask_b32_e32 v70, v199, v70, vcc
	v_cmp_lt_i32_e32 vcc, v170, v200
	v_add_u32_e32 v170, 41, v1
	s_nop 0
	v_cndmask_b32_e32 v87, v199, v87, vcc
	v_cmp_lt_i32_e32 vcc, v170, v200
	v_add_u32_e32 v170, 10, v1
	s_nop 0
	v_cndmask_b32_e32 v71, v199, v71, vcc
	v_cmp_lt_i32_e32 vcc, v170, v200
	v_add_u32_e32 v170, 42, v1
	s_nop 0
	v_cndmask_b32_e32 v88, v199, v88, vcc
	v_cmp_lt_i32_e32 vcc, v170, v200
	v_add_u32_e32 v170, 11, v1
	s_nop 0
	v_cndmask_b32_e32 v72, v199, v72, vcc
	v_cmp_lt_i32_e32 vcc, v170, v200
	v_add_u32_e32 v170, 43, v1
	s_nop 0
	v_cndmask_b32_e32 v89, v199, v89, vcc
	v_cmp_lt_i32_e32 vcc, v170, v200
	v_add_u32_e32 v170, 16, v1
	s_nop 0
	v_cndmask_b32_e32 v73, v199, v73, vcc
	v_cmp_lt_i32_e32 vcc, v170, v200
	v_add_u32_e32 v170, 48, v1
	s_nop 0
	v_cndmask_b32_e32 v90, v199, v90, vcc
	v_cmp_lt_i32_e32 vcc, v170, v200
	v_add_u32_e32 v170, 17, v1
	s_nop 0
	v_cndmask_b32_e32 v74, v199, v74, vcc
	v_cmp_lt_i32_e32 vcc, v170, v200
	v_add_u32_e32 v170, 49, v1
	s_nop 0
	v_cndmask_b32_e32 v91, v199, v91, vcc
	v_cmp_lt_i32_e32 vcc, v170, v200
	v_add_u32_e32 v170, 18, v1
	s_nop 0
	v_cndmask_b32_e32 v75, v199, v75, vcc
	v_cmp_lt_i32_e32 vcc, v170, v200
	v_add_u32_e32 v170, 50, v1
	s_nop 0
	v_cndmask_b32_e32 v92, v199, v92, vcc
	v_cmp_lt_i32_e32 vcc, v170, v200
	v_add_u32_e32 v170, 19, v1
	s_nop 0
	v_cndmask_b32_e32 v76, v199, v76, vcc
	v_cmp_lt_i32_e32 vcc, v170, v200
	v_add_u32_e32 v170, 51, v1
	s_nop 0
	v_cndmask_b32_e32 v93, v199, v93, vcc
	v_cmp_lt_i32_e32 vcc, v170, v200
	v_add_u32_e32 v170, 24, v1
	s_nop 0
	v_cndmask_b32_e32 v77, v199, v77, vcc
	v_cmp_lt_i32_e32 vcc, v170, v200
	v_add_u32_e32 v170, 56, v1
	s_nop 0
	v_cndmask_b32_e32 v94, v199, v94, vcc
	v_cmp_lt_i32_e32 vcc, v170, v200
	v_add_u32_e32 v170, 25, v1
	s_nop 0
	v_cndmask_b32_e32 v78, v199, v78, vcc
	v_cmp_lt_i32_e32 vcc, v170, v200
	v_add_u32_e32 v170, 57, v1
	s_nop 0
	v_cndmask_b32_e32 v95, v199, v95, vcc
	v_cmp_lt_i32_e32 vcc, v170, v200
	v_add_u32_e32 v170, 26, v1
	s_nop 0
	v_cndmask_b32_e32 v79, v199, v79, vcc
	v_cmp_lt_i32_e32 vcc, v170, v200
	v_add_u32_e32 v170, 58, v1
	s_nop 0
	v_cndmask_b32_e32 v96, v199, v96, vcc
	v_cmp_lt_i32_e32 vcc, v170, v200
	v_add_u32_e32 v170, 27, v1
	v_add_u32_e32 v1, 59, v1
	v_cndmask_b32_e32 v80, v199, v80, vcc
	v_cmp_lt_i32_e32 vcc, v170, v200
	s_nop 1
	v_cndmask_b32_e32 v97, v199, v97, vcc
	v_cmp_lt_i32_e32 vcc, v1, v200
	s_nop 1
	v_cndmask_b32_e32 v81, v199, v81, vcc
